# v90 + routing: the two stores that need the position atomic's result are deferred by one token so the atomic round trip overlaps the next token's selection
# speedup vs baseline: 1.0034x; 1.0034x over previous
.LBB0_578:
	s_or_b64 exec, exec, s[0:1]
	s_add_u32 s40, s70, 0x5440
	s_addc_u32 s41, s71, 0
	s_add_u32 s0, s70, 0x1260d500
	s_addc_u32 s1, s71, 0
	v_writelane_b32 v253, s0, 55
	s_waitcnt lgkmcnt(0)
	s_barrier
	v_writelane_b32 v253, s1, 56
	s_add_u32 s0, s70, 0x1268d500
	s_addc_u32 s1, s71, 0
	v_writelane_b32 v253, s0, 57
	v_mov_b32_e32 v1, 0
	s_nop 0
	v_writelane_b32 v253, s1, 58
	s_add_u32 s0, s70, 0x1270d500
	s_addc_u32 s1, s71, 0
	v_writelane_b32 v253, s0, 59
	v_mov_b32_e32 v3, 0
	s_movk_i32 s33, 0x4000
	v_writelane_b32 v253, s1, 60
	s_add_u32 s0, s70, 0x1278d500
	s_addc_u32 s1, s71, 0
	v_writelane_b32 v253, s0, 61
	s_nop 1
	v_writelane_b32 v253, s1, 62
	s_getreg_b32 s0, hwreg(HW_REG_HW_ID, 0, 6)
	s_lshl_b32 s0, s0, 2
	s_add_i32 s0, s0, 0x27000
	v_mov_b32_e32 v0, s0
	ds_read_b32 v0, v0
	s_waitcnt lgkmcnt(0)
	v_readfirstlane_b32 s0, v0
	v_mbcnt_lo_u32_b32 v0, -1, v1
	v_mbcnt_hi_u32_b32 v0, -1, v0
	v_lshl_or_b32 v0, s0, 6, v0
	s_getreg_b32 s0, hwreg(HW_REG_HW_ID, 0, 6)
	s_lshl_b32 s0, s0, 2
	s_add_i32 s0, s0, 0x27000
	v_mov_b32_e32 v1, s0
	ds_read_b32 v2, v1
	v_mov_b32_e32 v1, 0
	s_waitcnt lgkmcnt(0)
	v_readfirstlane_b32 s0, v2
	v_mbcnt_lo_u32_b32 v2, -1, v3
	v_mbcnt_hi_u32_b32 v2, -1, v2
	v_lshl_or_b32 v2, s0, 6, v2
	v_readlane_b32 s0, v253, 30
	v_ashrrev_i32_e32 v8, 6, v2
	s_nop 0
	v_add_u32_e32 v2, s0, v8
	v_cmp_gt_i32_e32 vcc, s33, v2
	s_mov_b64 s[98:99], 0
	v_mov_b32_e32 v73, 0
	s_and_saveexec_b64 s[44:45], vcc
	s_cbranch_execz .LBB0_667
	v_ashrrev_i32_e32 v3, 31, v2
	v_readlane_b32 s2, v253, 53
	v_and_b32_e32 v22, 63, v0
	v_lshlrev_b64 v[4:5], 10, v[2:3]
	v_readlane_b32 s3, v253, 54
	v_lshlrev_b32_e32 v0, 2, v22
	v_readlane_b32 s12, v253, 4
	v_lshl_add_u64 v[4:5], s[2:3], 0, v[4:5]
	v_lshl_add_u64 v[4:5], v[4:5], 0, v[0:1]
	global_load_dword v24, v[4:5], off
	global_load_dword v29, v[4:5], off offset:256
	global_load_dword v30, v[4:5], off offset:512
	global_load_dword v9, v[4:5], off offset:768
	v_readlane_b32 s13, v253, 5
	v_xor_b32_e32 v3, 64, v0
	v_xor_b32_e32 v23, 0x80, v0
	v_lshl_add_u64 v[4:5], s[12:13], 0, v[0:1]
	global_load_dword v61, v[4:5], off
	global_load_dword v62, v[4:5], off offset:256
	global_load_dword v63, v[4:5], off offset:512
	global_load_dword v64, v[4:5], off offset:768
	v_lshl_add_u64 v[6:7], s[2:3], 0, v[0:1]
	s_lshl_b32 s2, s72, 6
	v_lshlrev_b32_e32 v0, 3, v8
	v_readlane_b32 s14, v253, 6
	v_readlane_b32 s15, v253, 7
	v_readlane_b32 s16, v253, 8
	v_readlane_b32 s17, v253, 9
	v_readlane_b32 s18, v253, 10
	v_readlane_b32 s19, v253, 11
	v_readlane_b32 s20, v253, 12
	v_readlane_b32 s21, v253, 13
	v_readlane_b32 s22, v253, 14
	v_readlane_b32 s23, v253, 15
	v_readlane_b32 s24, v253, 16
	v_readlane_b32 s25, v253, 17
	v_add3_u32 v8, s2, v0, v22
	v_readlane_b32 s2, v253, 2
	v_cmp_gt_u32_e64 s[0:1], 32, v22
	v_cmp_lt_u32_e64 s[4:5], 31, v22
	v_cmp_lt_u32_e64 s[6:7], 7, v22
	v_cmp_gt_u32_e64 s[8:9], 8, v22
	v_cmp_eq_u32_e64 s[10:11], 0, v22
	v_cmp_eq_u32_e64 s[12:13], 1, v22
	v_cmp_eq_u32_e64 s[14:15], 2, v22
	v_cmp_eq_u32_e64 s[16:17], 3, v22
	v_cmp_eq_u32_e64 s[18:19], 4, v22
	v_cmp_eq_u32_e64 s[20:21], 5, v22
	v_cmp_eq_u32_e64 s[22:23], 6, v22
	v_cmp_eq_u32_e64 s[24:25], 7, v22
	s_lshl_b32 s52, s2, 6
	s_mov_b64 s[46:47], 0
	s_mov_b32 s53, 0xbfb8aa3b
	s_mov_b32 s54, 0x42ce8ed0
	s_mov_b32 s55, 0xc2b17218
	v_mov_b32_e32 v25, 0x7f800000
	v_mov_b32_e32 v26, 0xff800000
	v_mov_b32_e32 v27, 1
	v_readlane_b32 s26, v253, 18
	v_readlane_b32 s27, v253, 19
	v_readlane_b32 s3, v253, 3
	s_waitcnt vmcnt(0)
	s_branch .LBB0_581

.LBB0_580:
	s_waitcnt vmcnt(5)
	s_or_b64 exec, exec, s[2:3]
	s_and_b64 s[2:3], exec, s[26:27]
	s_or_b64 s[46:47], s[2:3], s[46:47]
	v_add_u32_e32 v8, s52, v8
	v_mov_b32_e32 v2, v28
	v_mov_b32_e32 v9, v31
	s_andn2_b64 exec, exec, s[46:47]
	s_cbranch_execz .LBB0_667

.LBB0_657:
	v_mov_b32_e32 v0, s56
	v_cndmask_b32_e64 v0, 0, v0, s[10:11]
	v_mov_b32_e32 v9, s57
	v_cndmask_b32_e64 v0, v0, v9, s[12:13]
	v_mov_b32_e32 v9, s58
	v_cndmask_b32_e64 v0, v0, v9, s[14:15]
	v_mov_b32_e32 v9, s59
	v_cndmask_b32_e64 v0, v0, v9, s[16:17]
	v_mov_b32_e32 v9, s60
	v_cndmask_b32_e64 v0, v0, v9, s[18:19]
	v_mov_b32_e32 v9, s61
	v_cndmask_b32_e64 v0, v0, v9, s[20:21]
	v_mov_b32_e32 v9, s62
	v_cndmask_b32_e64 v0, v0, v9, s[22:23]
	v_mov_b32_e32 v9, s63
	v_cndmask_b32_e64 v0, v0, v9, s[24:25]
	v_lshlrev_b32_e32 v9, 2, v0
	v_and_b32_e32 v9, 0xfc, v9
	ds_bpermute_b32 v12, v9, v12
	ds_bpermute_b32 v13, v9, v13
	ds_bpermute_b32 v11, v9, v11
	ds_bpermute_b32 v9, v9, v10
	v_lshrrev_b32_e32 v14, 6, v0
	v_cmp_eq_u32_e32 vcc, 2, v14
	s_waitcnt lgkmcnt(2)
	s_nop 0
	v_cndmask_b32_e32 v10, v13, v12, vcc
	v_cmp_eq_u32_e32 vcc, 1, v14
	s_waitcnt lgkmcnt(1)
	s_nop 0
	v_cndmask_b32_e32 v10, v10, v11, vcc
	v_cmp_gt_u32_e32 vcc, 64, v0
	s_waitcnt lgkmcnt(0)
	s_nop 0
	v_cndmask_b32_e32 v10, v10, v9, vcc
	v_cndmask_b32_e64 v9, v10, 0, s[6:7]
	s_nop 1
	v_add_f32_dpp v9, v9, v9 quad_perm:[1,0,3,2] row_mask:0xf bank_mask:0xf bound_ctrl:1
	s_nop 1
	v_add_f32_dpp v9, v9, v9 quad_perm:[2,3,0,1] row_mask:0xf bank_mask:0xf bound_ctrl:1
	s_nop 1
	v_mov_b32_dpp v11, v9 row_half_mirror row_mask:0xf bank_mask:0xf bound_ctrl:1
	s_and_saveexec_b64 s[2:3], s[8:9]
	s_cbranch_execz .Lopt19_rt0_skip
	s_cmp_eq_u64 s[98:99], 0
	s_cbranch_scc1 .Lopt29_rt0_np
	s_waitcnt vmcnt(4)
	global_store_dword v[74:75], v72, off
	v_lshl_add_u64 v[76:77], v[72:73], 2, v[76:77]
	global_store_dword v[76:77], v78, off
	s_branch .Lopt29_rt0_go

.Lopt29_rt0_go:
	v_lshlrev_b32_e32 v12, 6, v0
	v_and_b32_e32 v12, 0xffffff00, v12
	v_and_b32_e32 v13, 3, v0
	v_lshl_or_b32 v12, v13, 5, v12
	v_mov_b32_e32 v13, 0
	v_lshl_add_u64 v[12:13], v[12:13], 0, s[40:41]
	global_atomic_add v72, v[12:13], v27, off sc0
	v_add_f32_e32 v11, v9, v11
	v_ashrrev_i32_e32 v9, 31, v8
	v_readlane_b32 s28, v253, 55
	v_lshlrev_b64 v[14:15], 2, v[8:9]
	v_readlane_b32 s29, v253, 56
	s_nop 1
	v_lshl_add_u64 v[16:17], s[28:29], 0, v[14:15]
	v_readlane_b32 s28, v253, 59
	v_readlane_b32 s29, v253, 60
	global_store_dword v[16:17], v0, off
	s_nop 0
	v_lshl_add_u64 v[16:17], s[28:29], 0, v[14:15]
	v_div_scale_f32 v9, s[28:29], v11, v11, v10
	v_rcp_f32_e32 v13, v9
	v_readlane_b32 s28, v253, 57
	v_readlane_b32 s29, v253, 58
	v_mov_b32_e32 v74, v16
	v_mov_b32_e32 v75, v17
	v_fma_f32 v16, -v9, v13, 1.0
	v_fmac_f32_e32 v13, v16, v13
	v_div_scale_f32 v16, vcc, v10, v11, v10
	v_mul_f32_e32 v17, v16, v13
	v_fma_f32 v18, -v9, v17, v16
	v_fmac_f32_e32 v17, v18, v13
	v_fma_f32 v9, -v9, v17, v16
	v_div_fmas_f32 v9, v9, v13, v17
	v_div_fixup_f32 v9, v9, v11, v10
	v_mul_f32_e32 v9, 0x40200000, v9
	v_lshl_add_u64 v[10:11], s[28:29], 0, v[14:15]
	v_readlane_b32 s28, v253, 61
	global_store_dword v[10:11], v9, off
	v_lshlrev_b64 v[10:11], 16, v[0:1]
	v_readlane_b32 s29, v253, 62
	s_nop 0
	v_lshl_add_u64 v[10:11], s[28:29], 0, v[10:11]
	v_mov_b32_e32 v76, v10
	v_mov_b32_e32 v77, v11
	v_mov_b32_e32 v78, v2
	s_mov_b64 s[98:99], exec
	s_branch .LBB0_580

.LBB0_667:
	s_or_b64 exec, exec, s[44:45]
	s_waitcnt vmcnt(0)
	s_and_saveexec_b64 s[100:101], s[98:99]
	global_store_dword v[74:75], v72, off
	v_lshl_add_u64 v[76:77], v[72:73], 2, v[76:77]
	global_store_dword v[76:77], v78, off
	s_mov_b64 exec, s[100:101]
	s_waitcnt vmcnt(0)
	s_barrier
	s_getreg_b32 s0, hwreg(HW_REG_HW_ID, 0, 6)
	s_lshl_b32 s0, s0, 2
	s_add_i32 s0, s0, 0x27000
	v_mov_b32_e32 v0, s0
	ds_read_b32 v0, v0
	v_mov_b32_e32 v1, 0
	s_waitcnt lgkmcnt(0)
	v_readfirstlane_b32 s0, v0
	v_mbcnt_lo_u32_b32 v0, -1, v1
	v_mbcnt_hi_u32_b32 v0, -1, v0
	v_lshl_or_b32 v0, s0, 6, v0
	s_nop 0
	v_cmp_eq_u32_e32 vcc, 0, v0
	s_and_saveexec_b64 s[0:1], vcc
	s_cbranch_execz .LBB0_719
	s_add_i32 s2, 0, 0x24430
	v_mov_b32_e32 v0, s2
	s_waitcnt vmcnt(0) expcnt(0) lgkmcnt(0)
	ds_read_b32 v2, v0
	s_add_i32 s2, 0, 0x24434
	v_mov_b32_e32 v0, s2
	ds_read_b32 v0, v0
	s_waitcnt lgkmcnt(1)
	v_cmp_ne_u32_e32 vcc, 0, v2
	s_cbranch_vccnz .LBB0_683
	v_readlane_b32 s6, v253, 0
	v_readlane_b32 s7, v253, 1
	s_load_dword s4, s[6:7], 0x14
	s_load_dwordx2 s[2:3], s[6:7], 0x4
	s_mov_b32 s17, 1
	v_mov_b32_e32 v16, 0
	s_waitcnt lgkmcnt(0)
	s_lshr_b32 s6, s4, 16
	s_and_b32 s4, s4, 0xffff
	s_cmp_lg_u32 s4, 0
	s_cselect_b64 s[4:5], -1, 0
	s_cmp_lg_u64 s[4:5], 0
	s_addc_u32 s2, s2, 0
	v_readlane_b32 s4, v253, 2
	v_readlane_b32 s5, v253, 3
	s_cmp_lg_u32 s6, 0
	s_mul_i32 s16, s2, s4
	s_cselect_b64 s[4:5], -1, 0
	s_cmp_lg_u64 s[4:5], 0
	s_addc_u32 s2, s3, 0
	s_mul_i32 s16, s16, s2
	s_add_u32 s2, s70, 0x1000
	s_addc_u32 s3, s71, 0
	s_add_u32 s4, s70, 0x1100
	s_addc_u32 s5, s71, 0
	s_add_u32 s6, s70, 0x1200
	s_addc_u32 s7, s71, 0
	s_add_u32 s8, s70, 0x1300
	s_addc_u32 s9, s71, 0
	s_branch .LBB0_671

.LBB0_2160:
	s_or_b64 exec, exec, s[0:1]
	s_waitcnt lgkmcnt(0)
	s_barrier
	s_add_u32 s30, s70, 0x9440
	s_getreg_b32 s0, hwreg(HW_REG_HW_ID, 0, 6)
	s_addc_u32 s31, s71, 0
	s_lshl_b32 s0, s0, 2
	s_add_i32 s0, s0, 0x27000
	v_mov_b32_e32 v0, s0
	ds_read_b32 v0, v0
	v_mov_b32_e32 v1, 0
	v_mov_b32_e32 v3, 0
	s_movk_i32 s33, 0x4000
	s_waitcnt lgkmcnt(0)
	v_readfirstlane_b32 s0, v0
	v_mbcnt_lo_u32_b32 v0, -1, v1
	v_mbcnt_hi_u32_b32 v0, -1, v0
	v_lshl_or_b32 v0, s0, 6, v0
	s_getreg_b32 s0, hwreg(HW_REG_HW_ID, 0, 6)
	s_lshl_b32 s0, s0, 2
	s_add_i32 s0, s0, 0x27000
	v_mov_b32_e32 v1, s0
	ds_read_b32 v2, v1
	v_mov_b32_e32 v1, 0
	s_waitcnt lgkmcnt(0)
	v_readfirstlane_b32 s0, v2
	v_mbcnt_lo_u32_b32 v2, -1, v3
	v_mbcnt_hi_u32_b32 v2, -1, v2
	v_lshl_or_b32 v2, s0, 6, v2
	v_readlane_b32 s0, v253, 30
	v_ashrrev_i32_e32 v8, 6, v2
	s_nop 0
	v_add_u32_e32 v2, s0, v8
	v_cmp_gt_i32_e32 vcc, s33, v2
	s_mov_b64 s[98:99], 0
	v_mov_b32_e32 v73, 0
	s_and_saveexec_b64 s[34:35], vcc
	s_cbranch_execz .LBB0_2249
	v_ashrrev_i32_e32 v3, 31, v2
	v_readlane_b32 s24, v253, 53
	v_and_b32_e32 v22, 63, v0
	v_lshlrev_b64 v[4:5], 10, v[2:3]
	v_readlane_b32 s25, v253, 54
	v_lshlrev_b32_e32 v0, 2, v22
	v_readlane_b32 s8, v253, 4
	v_lshl_add_u64 v[4:5], s[24:25], 0, v[4:5]
	v_lshl_add_u64 v[4:5], v[4:5], 0, v[0:1]
	global_load_dword v28, v[4:5], off
	global_load_dword v29, v[4:5], off offset:256
	global_load_dword v30, v[4:5], off offset:512
	global_load_dword v31, v[4:5], off offset:768
	v_readlane_b32 s9, v253, 5
	v_xor_b32_e32 v3, 64, v0
	v_xor_b32_e32 v23, 0x80, v0
	v_lshl_add_u64 v[4:5], s[8:9], 0, v[0:1]
	global_load_dword v61, v[4:5], off offset:1024
	global_load_dword v62, v[4:5], off offset:1280
	global_load_dword v63, v[4:5], off offset:1536
	global_load_dword v64, v[4:5], off offset:1792
	v_lshl_add_u64 v[6:7], s[24:25], 0, v[0:1]
	s_lshl_b32 s24, s72, 6
	v_lshlrev_b32_e32 v0, 3, v8
	v_readlane_b32 s10, v253, 6
	v_readlane_b32 s11, v253, 7
	v_readlane_b32 s12, v253, 8
	v_readlane_b32 s13, v253, 9
	v_readlane_b32 s14, v253, 10
	v_readlane_b32 s15, v253, 11
	v_readlane_b32 s16, v253, 12
	v_readlane_b32 s17, v253, 13
	v_readlane_b32 s18, v253, 14
	v_readlane_b32 s19, v253, 15
	v_readlane_b32 s20, v253, 16
	v_readlane_b32 s21, v253, 17
	v_readlane_b32 s22, v253, 18
	v_readlane_b32 s23, v253, 19
	v_add3_u32 v8, s24, v0, v22
	v_readlane_b32 s24, v253, 2
	v_cmp_gt_u32_e64 s[0:1], 32, v22
	v_cmp_lt_u32_e64 s[2:3], 31, v22
	v_cmp_lt_u32_e64 s[4:5], 7, v22
	v_cmp_gt_u32_e64 s[6:7], 8, v22
	v_cmp_eq_u32_e64 s[8:9], 0, v22
	v_cmp_eq_u32_e64 s[10:11], 1, v22
	v_cmp_eq_u32_e64 s[12:13], 2, v22
	v_cmp_eq_u32_e64 s[14:15], 3, v22
	v_cmp_eq_u32_e64 s[16:17], 4, v22
	v_cmp_eq_u32_e64 s[18:19], 5, v22
	v_cmp_eq_u32_e64 s[20:21], 6, v22
	v_cmp_eq_u32_e64 s[22:23], 7, v22
	s_lshl_b32 s42, s24, 6
	s_mov_b64 s[36:37], 0
	s_movk_i32 s43, 0x3fff
	s_mov_b32 s44, 0xbfb8aa3b
	s_mov_b32 s45, 0x42ce8ed0
	s_mov_b32 s46, 0xc2b17218
	v_mov_b32_e32 v24, 0x7f800000
	v_mov_b32_e32 v25, 0xff800000
	s_mov_b32 s47, 0xff800000
	v_mov_b32_e32 v26, 1
	v_readlane_b32 s25, v253, 3
	s_waitcnt vmcnt(0)
	s_branch .LBB0_2163

.LBB0_2162:
	s_waitcnt vmcnt(5)
	s_or_b64 exec, exec, s[26:27]
	s_and_b64 s[24:25], exec, s[24:25]
	s_or_b64 s[36:37], s[24:25], s[36:37]
	v_add_u32_e32 v8, s42, v8
	v_mov_b32_e32 v2, v27
	s_andn2_b64 exec, exec, s[36:37]
	s_cbranch_execz .LBB0_2249

.LBB0_2239:
	v_mov_b32_e32 v0, s48
	v_cndmask_b32_e64 v0, 0, v0, s[8:9]
	v_mov_b32_e32 v9, s49
	v_cndmask_b32_e64 v0, v0, v9, s[10:11]
	v_mov_b32_e32 v9, s50
	v_cndmask_b32_e64 v0, v0, v9, s[12:13]
	v_mov_b32_e32 v9, s51
	v_cndmask_b32_e64 v0, v0, v9, s[14:15]
	v_mov_b32_e32 v9, s52
	v_cndmask_b32_e64 v0, v0, v9, s[16:17]
	v_mov_b32_e32 v9, s53
	v_cndmask_b32_e64 v0, v0, v9, s[18:19]
	v_mov_b32_e32 v9, s54
	v_cndmask_b32_e64 v0, v0, v9, s[20:21]
	v_mov_b32_e32 v9, s55
	v_cndmask_b32_e64 v0, v0, v9, s[22:23]
	v_lshlrev_b32_e32 v9, 2, v0
	v_and_b32_e32 v9, 0xfc, v9
	ds_bpermute_b32 v12, v9, v12
	ds_bpermute_b32 v13, v9, v13
	ds_bpermute_b32 v11, v9, v11
	ds_bpermute_b32 v9, v9, v10
	v_lshrrev_b32_e32 v14, 6, v0
	v_cmp_eq_u32_e32 vcc, 2, v14
	s_waitcnt lgkmcnt(2)
	s_nop 0
	v_cndmask_b32_e32 v10, v13, v12, vcc
	v_cmp_eq_u32_e32 vcc, 1, v14
	s_waitcnt lgkmcnt(1)
	s_nop 0
	v_cndmask_b32_e32 v10, v10, v11, vcc
	v_cmp_gt_u32_e32 vcc, 64, v0
	s_waitcnt lgkmcnt(0)
	s_nop 0
	v_cndmask_b32_e32 v10, v10, v9, vcc
	v_cndmask_b32_e64 v9, v10, 0, s[4:5]
	s_nop 1
	v_add_f32_dpp v9, v9, v9 quad_perm:[1,0,3,2] row_mask:0xf bank_mask:0xf bound_ctrl:1
	s_nop 1
	v_add_f32_dpp v9, v9, v9 quad_perm:[2,3,0,1] row_mask:0xf bank_mask:0xf bound_ctrl:1
	s_nop 1
	v_mov_b32_dpp v11, v9 row_half_mirror row_mask:0xf bank_mask:0xf bound_ctrl:1
	s_and_saveexec_b64 s[26:27], s[6:7]
	s_cbranch_execz .Lopt19_rt1_skip
	s_cmp_eq_u64 s[98:99], 0
	s_cbranch_scc1 .Lopt29_rt1_np
	s_waitcnt vmcnt(4)
	global_store_dword v[74:75], v72, off
	v_lshl_add_u64 v[76:77], v[72:73], 2, v[76:77]
	global_store_dword v[76:77], v78, off
	s_branch .Lopt29_rt1_go

.Lopt29_rt1_go:
	v_lshlrev_b32_e32 v12, 6, v0
	v_and_b32_e32 v12, 0xffffff00, v12
	v_and_b32_e32 v13, 3, v0
	v_lshl_or_b32 v12, v13, 5, v12
	v_mov_b32_e32 v13, 0
	v_lshl_add_u64 v[12:13], v[12:13], 0, s[30:31]
	global_atomic_add v72, v[12:13], v26, off sc0
	v_add_f32_e32 v11, v9, v11
	v_ashrrev_i32_e32 v9, 31, v8
	v_lshlrev_b64 v[16:17], 2, v[8:9]
	v_div_scale_f32 v9, s[28:29], v11, v11, v10
	v_rcp_f32_e32 v32, v9
	v_readlane_b32 s28, v253, 55
	v_readlane_b32 s29, v253, 56
	v_lshlrev_b64 v[14:15], 16, v[0:1]
	v_div_scale_f32 v13, vcc, v10, v11, v10
	v_lshl_add_u64 v[18:19], s[28:29], 0, v[16:17]
	global_store_dword v[18:19], v0, off
	v_fma_f32 v0, -v9, v32, 1.0
	v_readlane_b32 s28, v253, 59
	v_fmac_f32_e32 v32, v0, v32
	v_readlane_b32 s29, v253, 60
	v_mul_f32_e32 v0, v13, v32
	v_fma_f32 v18, -v9, v0, v13
	v_lshl_add_u64 v[20:21], s[28:29], 0, v[16:17]
	v_readlane_b32 s28, v253, 57
	v_readlane_b32 s29, v253, 58
	v_fmac_f32_e32 v0, v18, v32
	v_fma_f32 v9, -v9, v0, v13
	v_lshl_add_u64 v[16:17], s[28:29], 0, v[16:17]
	v_readlane_b32 s28, v253, 61
	v_div_fmas_f32 v0, v9, v32, v0
	v_readlane_b32 s29, v253, 62
	v_div_fixup_f32 v0, v0, v11, v10
	v_mul_f32_e32 v0, 0x40200000, v0
	v_lshl_add_u64 v[10:11], s[28:29], 0, v[14:15]
	global_store_dword v[16:17], v0, off
	v_mov_b32_e32 v74, v20
	v_mov_b32_e32 v75, v21
	v_mov_b32_e32 v76, v10
	v_mov_b32_e32 v77, v11
	v_mov_b32_e32 v78, v2
	s_mov_b64 s[98:99], exec
	s_branch .LBB0_2162

.LBB0_2249:
	s_or_b64 exec, exec, s[34:35]
	s_waitcnt vmcnt(0)
	s_and_saveexec_b64 s[100:101], s[98:99]
	global_store_dword v[74:75], v72, off
	v_lshl_add_u64 v[76:77], v[72:73], 2, v[76:77]
	global_store_dword v[76:77], v78, off
	s_mov_b64 exec, s[100:101]
	s_waitcnt vmcnt(0)
	s_barrier
	s_getreg_b32 s0, hwreg(HW_REG_HW_ID, 0, 6)
	s_lshl_b32 s0, s0, 2
	s_add_i32 s0, s0, 0x27000
	v_mov_b32_e32 v0, s0
	ds_read_b32 v0, v0
	v_mov_b32_e32 v1, 0
	s_waitcnt lgkmcnt(0)
	v_readfirstlane_b32 s0, v0
	v_mbcnt_lo_u32_b32 v0, -1, v1
	v_mbcnt_hi_u32_b32 v0, -1, v0
	v_lshl_or_b32 v0, s0, 6, v0
	s_nop 0
	v_cmp_eq_u32_e32 vcc, 0, v0
	s_and_saveexec_b64 s[0:1], vcc
	s_cbranch_execz .LBB0_2301
	s_add_i32 s2, 0, 0x24430
	v_mov_b32_e32 v0, s2
	s_waitcnt vmcnt(0) expcnt(0) lgkmcnt(0)
	ds_read_b32 v2, v0
	s_add_i32 s2, 0, 0x24434
	v_mov_b32_e32 v0, s2
	ds_read_b32 v0, v0
	s_waitcnt lgkmcnt(1)
	v_cmp_ne_u32_e32 vcc, 0, v2
	s_cbranch_vccnz .LBB0_2265
	v_readlane_b32 s6, v253, 0
	v_readlane_b32 s7, v253, 1
	s_load_dword s4, s[6:7], 0x14
	s_load_dwordx2 s[2:3], s[6:7], 0x4
	s_mov_b32 s17, 1
	v_mov_b32_e32 v16, 0
	s_waitcnt lgkmcnt(0)
	s_lshr_b32 s6, s4, 16
	s_and_b32 s4, s4, 0xffff
	s_cmp_lg_u32 s4, 0
	s_cselect_b64 s[4:5], -1, 0
	s_cmp_lg_u64 s[4:5], 0
	s_addc_u32 s2, s2, 0
	v_readlane_b32 s4, v253, 2
	v_readlane_b32 s5, v253, 3
	s_cmp_lg_u32 s6, 0
	s_mul_i32 s16, s2, s4
	s_cselect_b64 s[4:5], -1, 0
	s_cmp_lg_u64 s[4:5], 0
	s_addc_u32 s2, s3, 0
	s_mul_i32 s16, s16, s2
	s_add_u32 s2, s70, 0x1000
	s_addc_u32 s3, s71, 0
	s_add_u32 s4, s70, 0x1100
	s_addc_u32 s5, s71, 0
	s_add_u32 s6, s70, 0x1200
	s_addc_u32 s7, s71, 0
	s_add_u32 s8, s70, 0x1300
	s_addc_u32 s9, s71, 0
	s_branch .LBB0_2253
